# speedup vs baseline: 1.0483x; 1.0329x over previous
_Z11main_kernelPKfPKiPK15HIP_vector_typeIjLj4EES0_PfS7_S2_i:
	v_and_b32_e32 v104, 0x3ff, v0
	s_mul_i32 s2, s2, 12
	v_readfirstlane_b32 s3, v104
	s_lshr_b32 s3, s3, 6
	s_add_i32 s2, s3, s2
	s_load_dwordx8 s[12:19], s[0:1], 0x0
	s_load_dwordx2 s[10:11], s[0:1], 0x30
	s_mul_i32 s2, s2, 0xf424
	s_mul_hi_u32 s4, s2, 0xaaaaaaab
	s_add_i32 s2, s2, 0xf424
	s_mul_hi_u32 s2, s2, 0xaaaaaaab
	s_lshr_b32 s42, s2, 11
	s_lshl_b32 s2, s3, 8
	v_and_b32_e32 v1, 15, v0
	v_bfe_u32 v112, v0, 4, 2
	s_lshr_b32 s44, s4, 11
	s_lshl_b32 s33, s3, 13
	s_add_i32 s43, s2, 0x20000
	s_waitcnt lgkmcnt(0)
	s_and_b32 s13, s13, 0xffff
	v_lshlrev_b32_e32 v105, 9, v112
	v_lshlrev_b32_e32 v2, 6, v112
	v_lshlrev_b32_e32 v3, 4, v1
	s_cmp_lt_u32 s44, s42
	s_mov_b32 s7, 0x20000
	v_bitop3_b32 v113, v2, v105, v3 bitop3:0xde
	s_mov_b32 s6, 0x1e848000
	s_cselect_b64 s[8:9], -1, 0
	v_lshlrev_b32_e32 v102, 2, v1
	v_lshlrev_b32_e32 v14, 4, v104
	v_mov_b32_e32 v15, 0
	v_lshl_add_u64 v[6:7], s[16:17], 0, v[14:15]
	v_add_co_u32_e32 v16, vcc, 0x3000, v6
	v_min_u32_e32 v6, 0x1ff, v104
	s_nop 0
	v_addc_co_u32_e32 v17, vcc, 0, v7, vcc
	v_lshlrev_b32_e32 v7, 2, v6
	global_load_dword v15, v7, s[10:11]
	global_load_dwordx4 v[2:5], v14, s[16:17]
	v_lshlrev_b32_e32 v18, 4, v6
	v_or_b32_e32 v19, 0x6000, v18
	global_load_dwordx4 v[6:9], v[16:17], off
	global_load_dwordx4 v[10:13], v19, s[16:17]
	v_min_u32_e32 v16, 0x17f, v104
	v_lshlrev_b32_e32 v16, 2, v16
	global_load_dword v17, v16, s[18:19]
	s_cmp_ge_u32 s44, s42
	s_cbranch_scc1 .Lmain_nodma
	s_lshl_b32 s2, s44, 13
	s_add_i32 m0, s33, 0x8000
	s_mov_b32 s4, s12
	s_mov_b32 s5, s13
	buffer_load_dwordx4 v113, s[4:7], s2 offen nt lds
	s_add_i32 m0, s33, 0x8400
	s_or_b32 s3, s2, 0x800
	buffer_load_dwordx4 v113, s[4:7], s3 offen nt lds
	s_add_i32 m0, s33, 0x8800
	s_or_b32 s3, s2, 0x1000
	buffer_load_dwordx4 v113, s[4:7], s3 offen nt lds
	s_add_i32 m0, s33, 0x8c00
	s_or_b32 s3, s2, 0x1800
	buffer_load_dwordx4 v113, s[4:7], s3 offen nt lds
	s_add_i32 m0, s33, 0x9000
	s_or_b32 s3, s2, 0x100
	buffer_load_dwordx4 v113, s[4:7], s3 offen nt lds
	s_add_i32 m0, s33, 0x9400
	s_or_b32 s3, s2, 0x900
	buffer_load_dwordx4 v113, s[4:7], s3 offen nt lds
	s_add_i32 m0, s33, 0x9800
	s_or_b32 s3, s2, 0x1100
	buffer_load_dwordx4 v113, s[4:7], s3 offen nt lds
	s_add_i32 m0, s33, 0x9c00
	s_or_b32 s2, s2, 0x1900
	buffer_load_dwordx4 v113, s[4:7], s2 offen nt lds
	s_lshl_b32 s2, s44, 6
	s_add_u32 s2, s14, s2
	s_addc_u32 s3, s15, 0
	s_mov_b32 m0, s43
	s_nop 0
	global_load_lds_dword v102, s[2:3]
.LBB1_2:
	s_load_dwordx2 s[2:3], s[0:1], 0x4c
	s_load_dwordx2 s[10:11], s[0:1], 0x28
	v_add_u32_e32 v16, 0x20c00, v16
	s_waitcnt lgkmcnt(0)
	s_and_b32 s4, s3, 0xffff
	s_lshr_b32 s3, s2, 16
	s_and_b32 s2, s2, 0xffff
	s_mul_i32 s5, s3, s2
	s_bfe_i32 s5, s5, 0x180000
	s_mul_i32 s4, s5, s4
	s_add_i32 s5, s4, 63
	s_bitcmp1_b32 exec_hi, 0
	s_waitcnt vmcnt(9)
	v_cmp_ne_u32_e32 vcc, 0, v15
	ds_write_b128 v14, v[2:5]
	s_nop 0
	v_cndmask_b32_e64 v2, 0, 1, vcc
	ds_write_b128 v14, v[6:9] offset:12288
	ds_write_b128 v18, v[10:13] offset:24576
	v_or_b32_dpp v2, v2, v2 row_shl:1 row_mask:0xf bank_mask:0xf bound_ctrl:1
	ds_write_b32 v16, v17
	s_nop 0
	v_or_b32_dpp v2, v2, v2 row_shl:2 row_mask:0xf bank_mask:0xf bound_ctrl:1
	s_nop 1
	v_or_b32_dpp v2, v2, v2 row_shl:4 row_mask:0xf bank_mask:0xf bound_ctrl:1
	s_nop 1
	v_or_b32_dpp v2, v2, v2 row_shl:8 row_mask:0xf bank_mask:0xf bound_ctrl:1
	s_nop 1
	v_mov_b32_dpp v3, v2 wave_shl:1 row_mask:0xf bank_mask:0xf bound_ctrl:1
	s_nop 1
	v_or_b32_dpp v2, v3, v2 row_mirror row_mask:0xf bank_mask:0xf bound_ctrl:1
	s_nop 0
	v_readlane_b32 s4, v2, 32
	v_readlane_b32 s16, v2, 0
	s_cselect_b32 s4, s4, 0
	s_or_b32 s4, s4, s16
	s_andn2_b32 s5, s5, 63
	s_cmp_eq_u32 s5, 64
	s_cbranch_scc1 .LBB1_9
	v_mbcnt_lo_u32_b32 v2, -1, 0
	v_mbcnt_hi_u32_b32 v4, -1, v2
	v_bfe_u32 v2, v0, 10, 10
	v_bfe_u32 v3, v0, 20, 10
	v_mad_u32_u24 v2, v3, s3, v2
	v_mad_u64_u32 v[2:3], s[2:3], v2, s2, v[104:105]
	v_lshrrev_b32_e32 v3, 6, v2
	v_or_b32_e32 v3, v4, v3
	v_cmp_eq_u32_e32 vcc, 0, v3
	s_and_saveexec_b64 s[2:3], vcc
	v_mov_b32_e32 v3, 0x21200
	v_mov_b32_e32 v5, s4
	ds_write_b32 v3, v5
	s_or_b64 exec, exec, s[2:3]
	v_cmp_eq_u32_e32 vcc, 0, v4
	v_cmp_lt_u32_e64 s[2:3], 63, v2
	s_and_b64 s[16:17], s[2:3], vcc
	s_waitcnt lgkmcnt(0)
	s_barrier
	s_and_saveexec_b64 s[2:3], s[16:17]
	s_cbranch_execz .LBB1_8
	v_mbcnt_lo_u32_b32 v2, exec_lo, 0
	v_mbcnt_hi_u32_b32 v2, exec_hi, v2
	v_cmp_eq_u32_e32 vcc, 0, v2
	s_and_b64 exec, exec, vcc
	v_mov_b32_e32 v2, 0x21200
	v_mov_b32_e32 v3, s4
	ds_or_b32 v2, v3

.LBB1_12:
	s_mov_b32 s0, s44
	s_add_i32 s44, s44, 1
	s_cmp_ge_u32 s44, s42
	s_cselect_b64 s[22:23], -1, 0
	s_cmp_lt_u32 s44, s42
	s_cselect_b32 s2, s44, s0
	s_waitcnt vmcnt(0)
	s_lshl_b32 s0, s2, 4
	s_mov_b32 s1, s17
	s_mov_b32 m0, s43
	ds_read_b128 v[76:79], v119 offset:32768
	ds_read_b128 v[80:83], v119 offset:36864
	ds_read_b128 v[84:87], v120 offset:32768
	ds_read_b128 v[88:91], v120 offset:36864
	ds_read_b128 v[92:95], v121
	ds_read_b128 v[96:99], v121 offset:4096
	ds_read_b128 v[128:131], v122
	ds_read_b128 v[132:135], v122 offset:4096
	ds_read_b128 v[72:75], v123
	s_waitcnt lgkmcnt(0)
	v_lshl_add_u64 v[70:71], s[0:1], 2, v[2:3]
	global_load_lds_dword v[70:71], off
	s_waitcnt lgkmcnt(0)
	v_cvt_pk_bf16_f32 v76, v76, v77
	v_cvt_pk_bf16_f32 v77, v78, v79
	v_cvt_pk_bf16_f32 v78, v84, v85
	v_cvt_pk_bf16_f32 v79, v86, v87
	v_cvt_pk_bf16_f32 v84, v92, v93
	v_cvt_pk_bf16_f32 v85, v94, v95
	v_cvt_pk_bf16_f32 v86, v128, v129
	v_cvt_pk_bf16_f32 v87, v130, v131
	v_cvt_pk_bf16_f32 v80, v80, v81
	v_cvt_pk_bf16_f32 v81, v82, v83
	v_cvt_pk_bf16_f32 v82, v88, v89
	v_cvt_pk_bf16_f32 v83, v90, v91
	v_cvt_pk_bf16_f32 v128, v96, v97
	v_cvt_pk_bf16_f32 v129, v98, v99
	v_cvt_pk_bf16_f32 v130, v132, v133
	v_cvt_pk_bf16_f32 v131, v134, v135
	ds_read_b128 v[88:91], v115
	ds_read_b128 v[92:95], v115 offset:1024
	ds_read_b128 v[96:99], v115 offset:2048
	ds_read_b128 v[132:135], v115 offset:3072
	s_lshl_b32 s0, s2, 13
	s_cmp_lt_u32 s44, s42
	s_cselect_b32 s0, s0, 0x1e848000
	s_waitcnt lgkmcnt(0)
	v_mfma_f32_16x16x32_bf16 v[88:91], v[76:79], v[88:91], v[36:39]
	v_mfma_f32_16x16x32_bf16 v[96:99], v[76:79], v[96:99], v[44:47]
	v_mfma_f32_16x16x32_bf16 v[92:95], v[76:79], v[92:95], v[40:43]
	v_mfma_f32_16x16x32_bf16 v[132:135], v[76:79], v[132:135], v[48:51]
	s_mov_b32 m0, s47
	s_nop 0
	buffer_load_dwordx4 v113, s[12:15], s0 offen nt lds
	ds_read_b128 v[136:139], v115 offset:4096
	ds_read_b128 v[140:143], v115 offset:5120
	ds_read_b128 v[144:147], v115 offset:6144
	ds_read_b128 v[148:151], v115 offset:7168
	s_waitcnt lgkmcnt(0)
	v_mfma_f32_16x16x32_bf16 v[136:139], v[76:79], v[136:139], v[52:55]
	v_mfma_f32_16x16x32_bf16 v[140:143], v[76:79], v[140:143], v[56:59]
	v_mfma_f32_16x16x32_bf16 v[144:147], v[76:79], v[144:147], v[60:63]
	v_mfma_f32_16x16x32_bf16 v[76:79], v[76:79], v[148:151], v[64:67]
	s_or_b32 s1, s0, 0x800
	s_mov_b32 m0, s48
	s_nop 0
	buffer_load_dwordx4 v113, s[12:15], s1 offen nt lds
	ds_read_b128 v[148:151], v115 offset:8192
	ds_read_b128 v[152:155], v115 offset:9216
	s_waitcnt lgkmcnt(0)
	v_mfma_f32_16x16x32_bf16 v[88:91], v[84:87], v[148:151], v[88:91]
	v_mfma_f32_16x16x32_bf16 v[92:95], v[84:87], v[152:155], v[92:95]
	ds_read_b128 v[148:151], v115 offset:10240
	ds_read_b128 v[152:155], v115 offset:11264
	s_waitcnt lgkmcnt(0)
	v_mfma_f32_16x16x32_bf16 v[96:99], v[84:87], v[148:151], v[96:99]
	v_mfma_f32_16x16x32_bf16 v[132:135], v[84:87], v[152:155], v[132:135]
	s_or_b32 s1, s0, 0x1000
	s_mov_b32 m0, s49
	s_nop 0
	buffer_load_dwordx4 v113, s[12:15], s1 offen nt lds
	ds_read_b128 v[148:151], v115 offset:12288
	ds_read_b128 v[152:155], v115 offset:13312
	s_waitcnt lgkmcnt(0)
	v_mfma_f32_16x16x32_bf16 v[136:139], v[84:87], v[148:151], v[136:139]
	v_mfma_f32_16x16x32_bf16 v[140:143], v[84:87], v[152:155], v[140:143]
	ds_read_b128 v[148:151], v115 offset:14336
	ds_read_b128 v[152:155], v115 offset:15360
	s_waitcnt lgkmcnt(0)
	v_mfma_f32_16x16x32_bf16 v[76:79], v[84:87], v[152:155], v[76:79]
	v_mfma_f32_16x16x32_bf16 v[144:147], v[84:87], v[148:151], v[144:147]
	s_or_b32 s1, s0, 0x1800
	s_mov_b32 m0, s50
	s_nop 0
	buffer_load_dwordx4 v113, s[12:15], s1 offen nt lds
	ds_read_b128 v[84:87], v115 offset:16384
	ds_read_b128 v[148:151], v115 offset:17408
	s_or_b32 s1, s0, 0x100
	s_waitcnt lgkmcnt(0)
	v_mfma_f32_16x16x32_bf16 v[84:87], v[80:83], v[84:87], v[88:91]
	v_mfma_f32_16x16x32_bf16 v[88:91], v[80:83], v[148:151], v[92:95]
	s_nop 2
	ds_read_b128 v[92:95], v115 offset:18432
	ds_read_b128 v[148:151], v115 offset:19456
	s_waitcnt lgkmcnt(0)
	v_mfma_f32_16x16x32_bf16 v[92:95], v[80:83], v[92:95], v[96:99]
	v_mfma_f32_16x16x32_bf16 v[132:135], v[80:83], v[148:151], v[132:135]
	s_mov_b32 m0, s51
	s_nop 0
	buffer_load_dwordx4 v113, s[12:15], s1 offen nt lds
	ds_read_b128 v[96:99], v115 offset:20480
	ds_read_b128 v[148:151], v115 offset:21504
	s_waitcnt lgkmcnt(0)
	v_mfma_f32_16x16x32_bf16 v[136:139], v[80:83], v[96:99], v[136:139]
	v_mfma_f32_16x16x32_bf16 v[140:143], v[80:83], v[148:151], v[140:143]
	ds_read_b128 v[96:99], v115 offset:22528
	ds_read_b128 v[148:151], v115 offset:23552
	s_waitcnt lgkmcnt(0)
	v_mfma_f32_16x16x32_bf16 v[76:79], v[80:83], v[148:151], v[76:79]
	v_mfma_f32_16x16x32_bf16 v[144:147], v[80:83], v[96:99], v[144:147]
	s_or_b32 s1, s0, 0x900
	s_mov_b32 m0, s52
	s_nop 0
	buffer_load_dwordx4 v113, s[12:15], s1 offen nt lds
	ds_read_b128 v[80:83], v115 offset:24576
	ds_read_b128 v[96:99], v115 offset:25600
	s_waitcnt lgkmcnt(0)
	v_mfma_f32_16x16x32_bf16 v[148:151], v[128:131], v[80:83], v[84:87]
	ds_read_b128 v[80:83], v115 offset:26624
	s_nop 1
	ds_read_b128 v[84:87], v115 offset:27648
	v_mfma_f32_16x16x32_bf16 v[152:155], v[128:131], v[96:99], v[88:91]
	s_waitcnt lgkmcnt(0)
	v_mfma_f32_16x16x32_bf16 v[96:99], v[128:131], v[80:83], v[92:95]
	v_mfma_f32_16x16x32_bf16 v[92:95], v[128:131], v[84:87], v[132:135]
	s_or_b32 s1, s0, 0x1100
	s_mov_b32 m0, s53
	s_nop 0
	buffer_load_dwordx4 v113, s[12:15], s1 offen nt lds
	ds_read_b128 v[80:83], v115 offset:28672
	ds_read_b128 v[84:87], v115 offset:29696
	s_waitcnt lgkmcnt(0)
	v_mfma_f32_16x16x32_bf16 v[88:91], v[128:131], v[80:83], v[136:139]
	ds_read_b128 v[80:83], v115 offset:30720
	ds_read_b128 v[132:135], v115 offset:31744
	v_mfma_f32_16x16x32_bf16 v[84:87], v[128:131], v[84:87], v[140:143]
	s_waitcnt lgkmcnt(0)
	v_mfma_f32_16x16x32_bf16 v[76:79], v[128:131], v[132:135], v[76:79]
	v_mfma_f32_16x16x32_bf16 v[80:83], v[128:131], v[80:83], v[144:147]
	s_or_b32 s0, s0, 0x1900
	s_mov_b32 m0, s54
	s_nop 0
	buffer_load_dwordx4 v113, s[12:15], s0 offen nt lds
	v_fma_f32 v70, v149, v149, 0
	v_fmac_f32_e32 v70, v153, v153
	v_fmac_f32_e32 v70, v97, v97
	v_fmac_f32_e32 v70, v93, v93
	v_fmac_f32_e32 v70, v89, v89
	v_fmac_f32_e32 v70, v85, v85
	v_fmac_f32_e32 v70, v81, v81
	v_fmac_f32_e32 v70, v77, v77
	v_fma_f32 v68, v148, v148, 0
	v_fmac_f32_e32 v68, v152, v152
	v_add_f32_dpp v70, v70, v70 quad_perm:[1,0,3,2] row_mask:0xf bank_mask:0xf bound_ctrl:1
	v_fmac_f32_e32 v68, v96, v96
	v_fmac_f32_e32 v68, v92, v92
	v_add_f32_dpp v70, v70, v70 quad_perm:[2,3,0,1] row_mask:0xf bank_mask:0xf bound_ctrl:1
	v_fmac_f32_e32 v68, v88, v88
	v_fmac_f32_e32 v68, v84, v84
	v_add_f32_dpp v70, v70, v70 row_half_mirror row_mask:0xf bank_mask:0xf bound_ctrl:1
	v_fmac_f32_e32 v68, v80, v80
	v_fmac_f32_e32 v68, v76, v76
	v_add_f32_dpp v70, v70, v70 row_mirror row_mask:0xf bank_mask:0xf bound_ctrl:1
	v_fmamk_f32 v70, v70, 0x3c000000, v124
	v_rsq_f32_e32 v127, v70
	v_fma_f32 v70, v150, v150, 0
	v_fmac_f32_e32 v70, v154, v154
	v_fmac_f32_e32 v70, v98, v98
	v_fmac_f32_e32 v70, v94, v94
	v_fmac_f32_e32 v70, v90, v90
	v_fmac_f32_e32 v70, v86, v86
	v_fmac_f32_e32 v70, v82, v82
	v_fmac_f32_e32 v70, v78, v78
	v_add_f32_dpp v68, v68, v68 quad_perm:[1,0,3,2] row_mask:0xf bank_mask:0xf bound_ctrl:1
	v_mul_f32_e32 v131, v127, v149
	v_add_f32_dpp v70, v70, v70 quad_perm:[1,0,3,2] row_mask:0xf bank_mask:0xf bound_ctrl:1
	v_add_f32_dpp v68, v68, v68 quad_perm:[2,3,0,1] row_mask:0xf bank_mask:0xf bound_ctrl:1
	v_mul_f32_e32 v81, v127, v81
	v_add_f32_dpp v70, v70, v70 quad_perm:[2,3,0,1] row_mask:0xf bank_mask:0xf bound_ctrl:1
	v_add_f32_dpp v68, v68, v68 row_half_mirror row_mask:0xf bank_mask:0xf bound_ctrl:1
	v_cmp_gt_u32_e64 s[0:1], s55, v72
	v_add_f32_dpp v70, v70, v70 row_half_mirror row_mask:0xf bank_mask:0xf bound_ctrl:1
	v_add_f32_dpp v68, v68, v68 row_mirror row_mask:0xf bank_mask:0xf bound_ctrl:1
	v_fmamk_f32 v68, v68, 0x3c000000, v124
	v_add_f32_dpp v70, v70, v70 row_mirror row_mask:0xf bank_mask:0xf bound_ctrl:1
	v_fmamk_f32 v70, v70, 0x3c000000, v124
	v_rsq_f32_e32 v130, v70
	v_fma_f32 v70, v151, v151, 0
	v_fmac_f32_e32 v70, v155, v155
	v_fmac_f32_e32 v70, v99, v99
	v_fmac_f32_e32 v70, v95, v95
	v_fmac_f32_e32 v70, v91, v91
	v_fmac_f32_e32 v70, v87, v87
	v_fmac_f32_e32 v70, v83, v83
	v_fmac_f32_e32 v70, v79, v79
	v_rsq_f32_e32 v68, v68
	v_mul_f32_e32 v98, v130, v98
	v_add_f32_dpp v70, v70, v70 quad_perm:[1,0,3,2] row_mask:0xf bank_mask:0xf bound_ctrl:1
	v_mul_f32_e32 v90, v130, v90
	v_mul_f32_e32 v111, v68, v148
	v_add_f32_dpp v110, v70, v70 quad_perm:[2,3,0,1] row_mask:0xf bank_mask:0xf bound_ctrl:1
	ds_read2_b32 v[70:71], v114 offset0:128 offset1:144
	ds_read2_b32 v[128:129], v125 offset1:16
	v_add_f32_dpp v110, v110, v110 row_half_mirror row_mask:0xf bank_mask:0xf bound_ctrl:1
	v_mul_f32_e32 v96, v68, v96
	v_mul_f32_e32 v92, v68, v92
	v_add_f32_dpp v110, v110, v110 row_mirror row_mask:0xf bank_mask:0xf bound_ctrl:1
	v_fmamk_f32 v110, v110, 0x3c000000, v124
	s_waitcnt lgkmcnt(0)
	v_fma_f32 v111, v111, v70, v128
	v_fma_f32 v131, v131, v70, v128
	v_exp_f32_e32 v111, v111
	v_exp_f32_e32 v131, v131
	v_rsq_f32_e32 v132, v110
	v_mul_f32_e32 v88, v68, v88
	v_add_f32_e32 v110, 1.0, v111
	v_add_f32_e32 v111, 1.0, v131
	v_mul_f32_e32 v131, v130, v150
	v_mul_f32_e32 v133, v132, v151
	v_fma_f32 v131, v131, v70, v128
	v_fma_f32 v70, v133, v70, v128
	v_exp_f32_e32 v131, v131
	v_exp_f32_e32 v70, v70
	v_rcp_f32_e32 v110, v110
	v_rcp_f32_e32 v111, v111
	v_add_f32_e32 v128, 1.0, v131
	v_add_f32_e32 v70, 1.0, v70
	v_rcp_f32_e32 v128, v128
	v_rcp_f32_e32 v70, v70
	v_mul_f32_e32 v131, v68, v152
	v_fma_f32 v131, v131, v71, v129
	v_cvt_pk_bf16_f32 v110, v110, v111
	v_cvt_pk_bf16_f32 v111, v128, v70
	v_mul_f32_e32 v128, v127, v153
	v_exp_f32_e32 v131, v131
	v_fma_f32 v128, v128, v71, v129
	v_exp_f32_e32 v128, v128
	v_mul_f32_e32 v99, v132, v99
	v_add_f32_e32 v70, 1.0, v131
	v_rcp_f32_e32 v133, v70
	v_add_f32_e32 v70, 1.0, v128
	v_mul_f32_e32 v131, v130, v154
	v_rcp_f32_e32 v134, v70
	v_mul_f32_e32 v70, v132, v155
	v_fma_f32 v131, v131, v71, v129
	v_fmac_f32_e32 v129, v70, v71
	v_exp_f32_e32 v135, v129
	ds_read2_b32 v[70:71], v114 offset0:160 offset1:176
	ds_read2_b32 v[128:129], v125 offset0:32 offset1:48
	v_exp_f32_e32 v131, v131
	v_mul_f32_e32 v91, v132, v91
	v_add_f32_e32 v135, 1.0, v135
	v_rcp_f32_e32 v135, v135
	s_waitcnt lgkmcnt(0)
	v_fma_f32 v96, v96, v70, v128
	v_exp_f32_e32 v136, v96
	v_mul_f32_e32 v96, v127, v97
	v_fma_f32 v96, v96, v70, v128
	v_exp_f32_e32 v97, v96
	v_fma_f32 v98, v98, v70, v128
	v_fma_f32 v70, v99, v70, v128
	v_exp_f32_e32 v98, v98
	v_exp_f32_e32 v70, v70
	v_add_f32_e32 v97, 1.0, v97
	v_cvt_pk_bf16_f32 v96, v133, v134
	v_add_f32_e32 v133, 1.0, v136
	v_rcp_f32_e32 v99, v97
	v_add_f32_e32 v97, 1.0, v98
	v_add_f32_e32 v70, 1.0, v70
	v_fma_f32 v92, v92, v71, v129
	v_rcp_f32_e32 v133, v133
	v_rcp_f32_e32 v128, v97
	v_rcp_f32_e32 v70, v70
	v_exp_f32_e32 v92, v92
	v_cvt_pk_bf16_f32 v98, v133, v99
	v_add_f32_e32 v131, 1.0, v131
	v_cvt_pk_bf16_f32 v99, v128, v70
	v_add_f32_e32 v70, 1.0, v92
	v_mul_f32_e32 v92, v127, v93
	v_fma_f32 v92, v92, v71, v129
	v_exp_f32_e32 v92, v92
	v_mul_f32_e32 v93, v130, v94
	v_fma_f32 v93, v93, v71, v129
	v_rcp_f32_e32 v131, v131
	v_exp_f32_e32 v93, v93
	v_rcp_f32_e32 v94, v70
	v_add_f32_e32 v70, 1.0, v92
	v_rcp_f32_e32 v128, v70
	v_mul_f32_e32 v70, v132, v95
	v_cvt_pk_bf16_f32 v97, v131, v135
	v_add_f32_e32 v131, 1.0, v93
	v_fmac_f32_e32 v129, v70, v71
	ds_read2_b32 v[70:71], v114 offset0:192 offset1:208
	ds_read2_b32 v[92:93], v125 offset0:64 offset1:80
	v_exp_f32_e32 v95, v129
	v_rcp_f32_e32 v129, v131
	v_mul_f32_e32 v84, v68, v84
	v_mul_f32_e32 v80, v68, v80
	s_waitcnt lgkmcnt(0)
	v_fma_f32 v88, v88, v70, v92
	v_exp_f32_e32 v131, v88
	v_mul_f32_e32 v88, v127, v89
	v_fma_f32 v88, v88, v70, v92
	v_exp_f32_e32 v89, v88
	v_fma_f32 v90, v90, v70, v92
	v_fma_f32 v70, v91, v70, v92
	v_exp_f32_e32 v90, v90
	v_exp_f32_e32 v70, v70
	v_add_f32_e32 v89, 1.0, v89
	v_cvt_pk_bf16_f32 v88, v94, v128
	v_add_f32_e32 v94, 1.0, v131
	v_rcp_f32_e32 v91, v89
	v_add_f32_e32 v89, 1.0, v90
	v_add_f32_e32 v70, 1.0, v70
	v_fma_f32 v84, v84, v71, v93
	v_rcp_f32_e32 v94, v94
	v_rcp_f32_e32 v92, v89
	v_rcp_f32_e32 v70, v70
	v_exp_f32_e32 v84, v84
	v_cvt_pk_bf16_f32 v90, v94, v91
	v_mul_f32_e32 v68, v68, v76
	v_cvt_pk_bf16_f32 v91, v92, v70
	v_add_f32_e32 v70, 1.0, v84
	v_mul_f32_e32 v84, v127, v85
	v_fma_f32 v84, v84, v71, v93
	v_mul_f32_e32 v85, v130, v86
	v_exp_f32_e32 v84, v84
	v_fma_f32 v85, v85, v71, v93
	v_exp_f32_e32 v85, v85
	v_rcp_f32_e32 v92, v70
	v_add_f32_e32 v70, 1.0, v84
	v_rcp_f32_e32 v84, v70
	v_add_f32_e32 v70, 1.0, v85
	v_mul_f32_e32 v85, v132, v87
	v_fmac_f32_e32 v93, v85, v71
	v_exp_f32_e32 v85, v93
	v_rcp_f32_e32 v93, v70
	ds_read2_b32 v[70:71], v114 offset0:224 offset1:240
	ds_read2_b32 v[86:87], v125 offset0:96 offset1:112
	v_mul_f32_e32 v76, v127, v77
	v_mul_f32_e32 v82, v130, v82
	v_mul_f32_e32 v83, v132, v83
	v_mul_f32_e32 v77, v130, v78
	s_waitcnt lgkmcnt(0)
	v_fma_f32 v76, v76, v71, v87
	v_mul_f32_e32 v78, v132, v79
	v_fma_f32 v80, v80, v70, v86
	v_fma_f32 v81, v81, v70, v86
	v_fma_f32 v82, v82, v70, v86
	v_fma_f32 v70, v83, v70, v86
	v_fma_f32 v68, v68, v71, v87
	v_exp_f32_e32 v76, v76
	v_fma_f32 v77, v77, v71, v87
	v_fmac_f32_e32 v87, v78, v71
	v_exp_f32_e32 v82, v82
	v_exp_f32_e32 v70, v70
	v_exp_f32_e32 v68, v68
	v_exp_f32_e32 v77, v77
	v_exp_f32_e32 v71, v87
	v_add_f32_e32 v76, 1.0, v76
	v_add_f32_e32 v82, 1.0, v82
	v_add_f32_e32 v70, 1.0, v70
	v_add_f32_e32 v68, 1.0, v68
	v_rcp_f32_e32 v78, v76
	v_add_f32_e32 v76, 1.0, v77
	v_add_f32_e32 v71, 1.0, v71
	v_rcp_f32_e32 v82, v82
	v_rcp_f32_e32 v70, v70
	v_rcp_f32_e32 v68, v68
	v_rcp_f32_e32 v79, v76
	v_rcp_f32_e32 v71, v71
	v_exp_f32_e32 v80, v80
	v_exp_f32_e32 v81, v81
	v_cvt_pk_bf16_f32 v77, v82, v70
	v_cvt_pk_bf16_f32 v78, v68, v78
	v_cvt_pk_bf16_f32 v79, v79, v71
	v_subrev_u32_e32 v68, s16, v72
	v_subrev_u32_e32 v70, s16, v73
	v_subrev_u32_e32 v71, s16, v74
	v_add_f32_e32 v95, 1.0, v95
	v_add_f32_e32 v85, 1.0, v85
	v_add_f32_e32 v80, 1.0, v80
	v_add_f32_e32 v81, 1.0, v81
	v_max3_u32 v68, v68, v70, v71
	v_subrev_u32_e32 v70, s16, v75
	v_rcp_f32_e32 v95, v95
	v_rcp_f32_e32 v85, v85
	v_rcp_f32_e32 v80, v80
	v_rcp_f32_e32 v81, v81
	v_max_u32_e32 v68, v68, v70
	v_cmp_gt_u32_e32 vcc, 16, v68
	s_cmp_eq_u64 vcc, -1
	s_cselect_b64 s[24:25], -1, 0
	s_cmp_lg_u64 vcc, -1
	v_cvt_pk_bf16_f32 v89, v129, v95
	v_cvt_pk_bf16_f32 v84, v92, v84
	v_cvt_pk_bf16_f32 v85, v93, v85
	v_cvt_pk_bf16_f32 v76, v80, v81
	s_cselect_b64 s[26:27], -1, 0
	v_cmp_gt_u32_e64 s[2:3], s55, v73
	v_cmp_gt_u32_e64 s[4:5], s55, v74
	v_cmp_gt_u32_e64 s[6:7], s55, v75
	s_mov_b32 s8, 0
	s_branch .LBB1_14

.Lmain_nodma:
	s_waitcnt vmcnt(0)
	s_branch .LBB1_2

_Z10enc_kernelPKfS0_PK15HIP_vector_typeIjLj4EES4_S4_S0_S0_S0_Pf:
	s_load_dwordx4 s[12:15], s[0:1], 0x0
	s_load_dwordx2 s[16:17], s[0:1], 0x10
	s_load_dwordx8 s[4:11], s[0:1], 0x28
	v_lshrrev_b32_e32 v56, 6, v0
	s_lshl_b32 s2, s2, 6
	v_lshl_or_b32 v47, v56, 4, s2
	v_and_b32_e32 v57, 15, v0
	v_or_b32_e32 v2, v47, v57
	v_ashrrev_i32_e32 v3, 31, v2
	s_waitcnt lgkmcnt(0)
	v_and_b32_e32 v119, 48, v0
	global_load_dwordx4 v[120:123], v119, s[4:5]
	global_load_dwordx4 v[124:127], v119, s[4:5] offset:64
	global_load_dwordx4 v[128:131], v119, s[4:5] offset:128
	global_load_dwordx4 v[132:135], v119, s[4:5] offset:192
	global_load_dwordx4 v[136:139], v119, s[4:5] offset:256
	global_load_dwordx4 v[140:143], v119, s[4:5] offset:320
	global_load_dwordx4 v[144:147], v119, s[4:5] offset:384
	global_load_dwordx4 v[148:151], v119, s[4:5] offset:448
	global_load_dwordx4 v[152:155], v119, s[6:7]
	global_load_dwordx4 v[156:159], v119, s[6:7] offset:64
	global_load_dwordx4 v[160:163], v119, s[6:7] offset:128
	global_load_dwordx4 v[164:167], v119, s[6:7] offset:192
	global_load_dwordx4 v[168:171], v119, s[6:7] offset:256
	global_load_dwordx4 v[172:175], v119, s[6:7] offset:320
	global_load_dwordx4 v[176:179], v119, s[8:9]
	global_load_dwordx4 v[180:183], v119, s[8:9] offset:64
	global_load_dwordx4 v[184:187], v119, s[8:9] offset:128
	global_load_dwordx4 v[188:191], v119, s[8:9] offset:192
	v_lshl_add_u64 v[4:5], v[2:3], 2, s[14:15]
	global_load_dword v46, v[4:5], off
	v_mov_b32_e32 v45, 0
	v_lshlrev_b64 v[2:3], 9, v[2:3]
	v_lshlrev_b32_e32 v44, 4, v0
	v_lshl_add_u64 v[2:3], s[12:13], 0, v[2:3]
	v_and_b32_e32 v48, 48, v0
	v_mov_b32_e32 v49, v45
	v_lshl_add_u64 v[4:5], s[16:17], 0, v[44:45]
	v_lshl_add_u64 v[42:43], v[2:3], 0, v[48:49]
	s_movk_i32 s0, 0x2000
	v_add_co_u32_e32 v2, vcc, s0, v4
	s_movk_i32 s0, 0x4000
	s_nop 0
	v_addc_co_u32_e32 v3, vcc, 0, v5, vcc
	v_add_co_u32_e32 v6, vcc, s0, v4
	s_movk_i32 s0, 0x6000
	s_nop 0
	v_addc_co_u32_e32 v7, vcc, 0, v5, vcc
	global_load_dwordx4 v[18:21], v44, s[16:17]
	global_load_dwordx4 v[22:25], v[2:3], off offset:-4096
	global_load_dwordx4 v[26:29], v[2:3], off
	global_load_dwordx4 v[30:33], v[6:7], off offset:-4096
	v_add_co_u32_e32 v2, vcc, s0, v4
	s_mov_b32 s0, 0x8000
	s_nop 0
	v_addc_co_u32_e32 v3, vcc, 0, v5, vcc
	global_load_dwordx4 v[34:37], v[6:7], off
	global_load_dwordx4 v[38:41], v[2:3], off offset:-4096
	v_add_co_u32_e32 v6, vcc, s0, v4
	s_mov_b32 s0, 0xa000
	s_nop 0
	v_addc_co_u32_e32 v7, vcc, 0, v5, vcc
	global_load_dwordx4 v[50:53], v[2:3], off
	global_load_dwordx4 v[58:61], v[6:7], off offset:-4096
	v_add_co_u32_e32 v2, vcc, s0, v4
	s_mov_b32 s0, 0xc000
	s_nop 0
	v_addc_co_u32_e32 v3, vcc, 0, v5, vcc
	global_load_dwordx4 v[62:65], v[6:7], off
	global_load_dwordx4 v[66:69], v[2:3], off offset:-4096
	v_add_co_u32_e32 v6, vcc, s0, v4
	s_mov_b32 s0, 0xe000
	s_nop 0
	v_addc_co_u32_e32 v7, vcc, 0, v5, vcc
	global_load_dwordx4 v[70:73], v[2:3], off
	global_load_dwordx4 v[74:77], v[6:7], off offset:-4096
	v_add_co_u32_e32 v2, vcc, s0, v4
	s_mov_b32 s0, 0x10000
	s_nop 0
	v_addc_co_u32_e32 v3, vcc, 0, v5, vcc
	v_add_co_u32_e32 v4, vcc, s0, v4
	global_load_dwordx4 v[78:81], v[6:7], off
	global_load_dwordx4 v[82:85], v[2:3], off offset:-4096
	v_addc_co_u32_e32 v5, vcc, 0, v5, vcc
	global_load_dwordx4 v[86:89], v[2:3], off
	global_load_dwordx4 v[90:93], v[4:5], off offset:-4096
	global_load_dwordx4 v[94:97], v[4:5], off
	global_load_dwordx4 v[98:101], v[42:43], off
	global_load_dwordx4 v[102:105], v[42:43], off offset:64
	global_load_dwordx4 v[106:109], v[42:43], off offset:128
	global_load_dwordx4 v[110:113], v[42:43], off offset:192
	global_load_dwordx4 v[10:13], v[42:43], off offset:256
	global_load_dwordx4 v[14:17], v[42:43], off offset:320
	s_nop 0
	global_load_dwordx4 v[2:5], v[42:43], off offset:384
	global_load_dwordx4 v[6:9], v[42:43], off offset:448
	v_or_b32_e32 v1, 0x10000, v44
	v_and_b32_e32 v49, 63, v0
	s_movk_i32 s0, 0x1040
	s_movk_i32 s2, 0x104
	v_cmp_gt_u32_e32 vcc, 16, v49
	s_waitcnt vmcnt(24)
	ds_write_b128 v44, v[18:21]
	s_waitcnt vmcnt(23)
	ds_write_b128 v44, v[22:25] offset:4096
	s_waitcnt vmcnt(22)
	ds_write_b128 v44, v[26:29] offset:8192
	s_waitcnt vmcnt(21)
	ds_write_b128 v44, v[30:33] offset:12288
	s_waitcnt vmcnt(20)
	ds_write_b128 v44, v[34:37] offset:16384
	s_waitcnt vmcnt(19)
	ds_write_b128 v44, v[38:41] offset:20480
	s_waitcnt vmcnt(18)
	ds_write_b128 v44, v[50:53] offset:24576
	s_waitcnt vmcnt(17)
	ds_write_b128 v44, v[58:61] offset:28672
	s_waitcnt vmcnt(16)
	ds_write_b128 v44, v[62:65] offset:32768
	s_waitcnt vmcnt(15)
	ds_write_b128 v44, v[66:69] offset:36864
	s_waitcnt vmcnt(14)
	ds_write_b128 v44, v[70:73] offset:40960
	s_waitcnt vmcnt(13)
	ds_write_b128 v44, v[74:77] offset:45056
	s_waitcnt vmcnt(12)
	ds_write_b128 v44, v[78:81] offset:49152
	s_waitcnt vmcnt(11)
	ds_write_b128 v44, v[82:85] offset:53248
	s_waitcnt vmcnt(10)
	ds_write_b128 v44, v[86:89] offset:57344
	s_waitcnt vmcnt(9)
	ds_write_b128 v44, v[90:93] offset:61440
	s_waitcnt vmcnt(8)
	ds_write_b128 v1, v[94:97]
	s_waitcnt lgkmcnt(0)
	s_barrier
	v_mov_b32_e32 v24, v120
	v_mov_b32_e32 v25, v121
	v_mov_b32_e32 v26, v122
	v_mov_b32_e32 v27, v123
	v_mov_b32_e32 v28, v124
	v_mov_b32_e32 v29, v125
	v_mov_b32_e32 v30, v126
	v_mov_b32_e32 v31, v127
	v_mov_b32_e32 v32, v128
	v_mov_b32_e32 v33, v129
	v_mov_b32_e32 v34, v130
	v_mov_b32_e32 v35, v131
	v_mov_b32_e32 v40, v132
	v_mov_b32_e32 v41, v133
	v_mov_b32_e32 v42, v134
	v_mov_b32_e32 v43, v135
	s_waitcnt vmcnt(0)
	v_pk_fma_f32 v[18:19], v[98:99], -2.0, v[46:47] op_sel_hi:[1,0,0]
	v_pk_fma_f32 v[20:21], v[100:101], -2.0, v[46:47] op_sel_hi:[1,0,0]
	v_pk_fma_f32 v[22:23], v[102:103], -2.0, v[46:47] op_sel_hi:[1,0,0]
	v_pk_fma_f32 v[36:37], v[104:105], -2.0, v[46:47] op_sel_hi:[1,0,0]
	v_pk_fma_f32 v[38:39], v[106:107], -2.0, v[46:47] op_sel_hi:[1,0,0]
	v_cvt_pk_bf16_f32 v18, v18, v19
	v_cvt_pk_bf16_f32 v19, v20, v21
	v_cvt_pk_bf16_f32 v20, v22, v23
	v_cvt_pk_bf16_f32 v21, v36, v37
	v_cvt_pk_bf16_f32 v22, v38, v39
	v_mov_b32_e32 v36, v136
	v_mov_b32_e32 v37, v137
	v_mov_b32_e32 v38, v138
	v_mov_b32_e32 v39, v139
	v_accvgpr_write_b32 a0, v152
	v_accvgpr_write_b32 a1, v153
	v_accvgpr_write_b32 a2, v154
	v_accvgpr_write_b32 a3, v155
	v_accvgpr_write_b32 a4, v160
	v_accvgpr_write_b32 a5, v161
	v_accvgpr_write_b32 a6, v162
	v_accvgpr_write_b32 a7, v163
	v_accvgpr_write_b32 a8, v176
	v_accvgpr_write_b32 a9, v177
	v_accvgpr_write_b32 a10, v178
	v_accvgpr_write_b32 a11, v179
	v_accvgpr_write_b32 a12, v184
	v_accvgpr_write_b32 a13, v185
	v_accvgpr_write_b32 a14, v186
	v_accvgpr_write_b32 a15, v187
	v_lshlrev_b32_e32 v44, 4, v49
	ds_read_b128 v[58:61], v44
	ds_read_b128 v[62:65], v44 offset:1024
	ds_read_b128 v[66:69], v44 offset:4096
	ds_read_b128 v[70:73], v44 offset:5120
	ds_read_b128 v[74:77], v44 offset:8192
	ds_read_b128 v[78:81], v44 offset:9216
	ds_read_b128 v[82:85], v44 offset:12288
	ds_read_b128 v[86:89], v44 offset:13312
	v_pk_fma_f32 v[50:51], v[108:109], -2.0, v[46:47] op_sel_hi:[1,0,0]
	v_pk_fma_f32 v[52:53], v[110:111], -2.0, v[46:47] op_sel_hi:[1,0,0]
	v_pk_fma_f32 v[54:55], v[112:113], -2.0, v[46:47] op_sel_hi:[1,0,0]
	v_cvt_pk_bf16_f32 v23, v50, v51
	v_pk_fma_f32 v[0:1], v[10:11], -2.0, v[46:47] op_sel_hi:[1,0,0]
	v_pk_fma_f32 v[12:13], v[12:13], -2.0, v[46:47] op_sel_hi:[1,0,0]
	v_cvt_pk_bf16_f32 v10, v0, v1
	v_cvt_pk_bf16_f32 v11, v12, v13
	v_pk_fma_f32 v[8:9], v[8:9], -2.0, v[46:47] op_sel_hi:[1,0,0]
	v_pk_mul_f32 v[24:25], v[46:47], v[24:25] op_sel_hi:[0,1]
	v_pk_mul_f32 v[26:27], v[46:47], v[26:27] op_sel_hi:[0,1]
	v_accvgpr_write_b32 a16, v24
	v_accvgpr_write_b32 a17, v25
	v_accvgpr_write_b32 a18, v26
	v_accvgpr_write_b32 a19, v27
	v_pk_mul_f32 v[24:25], v[46:47], v[28:29] op_sel_hi:[0,1]
	v_pk_mul_f32 v[26:27], v[46:47], v[30:31] op_sel_hi:[0,1]
	v_accvgpr_write_b32 a20, v24
	v_accvgpr_write_b32 a21, v25
	v_accvgpr_write_b32 a22, v26
	v_accvgpr_write_b32 a23, v27
	v_pk_mul_f32 v[24:25], v[46:47], v[32:33] op_sel_hi:[0,1]
	v_mov_b32_e32 v30, v140
	v_mov_b32_e32 v31, v141
	v_mov_b32_e32 v32, v142
	v_mov_b32_e32 v33, v143
	v_pk_mul_f32 v[26:27], v[46:47], v[34:35] op_sel_hi:[0,1]
	v_accvgpr_write_b32 a24, v24
	v_accvgpr_write_b32 a25, v25
	v_accvgpr_write_b32 a26, v26
	v_accvgpr_write_b32 a27, v27
	v_pk_mul_f32 v[26:27], v[46:47], v[42:43] op_sel_hi:[0,1]
	v_pk_mul_f32 v[24:25], v[46:47], v[40:41] op_sel_hi:[0,1]
	v_accvgpr_write_b32 a31, v27
	v_accvgpr_write_b32 a30, v26
	v_accvgpr_write_b32 a29, v25
	v_accvgpr_write_b32 a28, v24
	v_pk_fma_f32 v[26:27], v[14:15], -2.0, v[46:47] op_sel_hi:[1,0,0]
	v_pk_fma_f32 v[28:29], v[16:17], -2.0, v[46:47] op_sel_hi:[1,0,0]
	ds_read_b128 v[14:17], v44 offset:2048
	s_waitcnt lgkmcnt(8)
	v_mfma_f32_16x16x32_bf16 a[16:19], v[58:61], v[18:21], a[16:19]
	v_cvt_pk_bf16_f32 v24, v52, v53
	v_cvt_pk_bf16_f32 v25, v54, v55
	v_cvt_pk_bf16_f32 v12, v26, v27
	s_waitcnt lgkmcnt(2)
	v_mfma_f32_16x16x32_bf16 a[28:31], v[82:85], v[18:21], a[28:31]
	v_cvt_pk_bf16_f32 v13, v28, v29
	ds_read_b128 v[26:29], v44 offset:6144
	ds_read_b128 v[40:43], v44 offset:3072
	ds_read_b128 v[50:53], v44 offset:10240
	v_mfma_f32_16x16x32_bf16 a[16:19], v[62:65], v[22:25], a[16:19]
	v_fma_f32 v34, v2, -2.0, v46
	v_fma_f32 v35, v3, -2.0, v46
	v_pk_fma_f32 v[54:55], v[6:7], -2.0, v[46:47] op_sel_hi:[1,0,0]
	v_pk_mul_f32 v[32:33], v[46:47], v[32:33] op_sel_hi:[0,1]
	s_waitcnt lgkmcnt(3)
	v_mfma_f32_16x16x32_bf16 a[16:19], v[14:17], v[10:13], a[16:19]
	ds_read_b128 v[0:3], v44 offset:7168
	ds_read_b128 v[14:17], v44 offset:14336
	v_pk_mul_f32 v[30:31], v[46:47], v[30:31] op_sel_hi:[0,1]
	v_accvgpr_write_b32 a47, v33
	v_mfma_f32_16x16x32_bf16 a[28:31], v[86:89], v[22:25], a[28:31]
	v_accvgpr_write_b32 a46, v32
	v_accvgpr_write_b32 a45, v31
	v_accvgpr_write_b32 a44, v30
	s_waitcnt lgkmcnt(0)
	v_mfma_f32_16x16x32_bf16 a[28:31], v[14:17], v[10:13], a[28:31]
	s_nop 1
	v_mov_b32_e32 v14, v144
	v_mov_b32_e32 v15, v145
	v_mov_b32_e32 v16, v146
	v_mov_b32_e32 v17, v147
	ds_read_b128 v[30:33], v44 offset:23552
	v_accvgpr_write_b32 a56, v156
	v_accvgpr_write_b32 a57, v157
	v_accvgpr_write_b32 a58, v158
	v_accvgpr_write_b32 a59, v159
	v_mfma_f32_16x16x32_bf16 a[20:23], v[66:69], v[18:21], a[20:23]
	v_accvgpr_write_b32 a32, v168
	v_accvgpr_write_b32 a33, v169
	v_accvgpr_write_b32 a34, v170
	v_accvgpr_write_b32 a35, v171
	v_accvgpr_write_b32 a40, v172
	v_accvgpr_write_b32 a41, v173
	v_accvgpr_write_b32 a42, v174
	v_accvgpr_write_b32 a43, v175
	v_mfma_f32_16x16x32_bf16 a[20:23], v[70:73], v[22:25], a[20:23]
	v_mfma_f32_16x16x32_bf16 a[20:23], v[26:29], v[10:13], a[20:23]
	v_fma_f32 v28, v4, -2.0, v46
	v_fma_f32 v29, v5, -2.0, v46
	v_cvt_pk_bf16_f32 v26, v34, v35
	v_cvt_pk_bf16_f32 v27, v28, v29
	v_cvt_pk_bf16_f32 v28, v54, v55
	v_cvt_pk_bf16_f32 v29, v8, v9
	v_mfma_f32_16x16x32_bf16 a[24:27], v[74:77], v[18:21], a[24:27]
	ds_read_b128 v[4:7], v44 offset:11264
	v_pk_mul_f32 v[34:35], v[46:47], v[36:37] op_sel_hi:[0,1]
	v_pk_mul_f32 v[36:37], v[46:47], v[38:39] op_sel_hi:[0,1]
	v_mfma_f32_16x16x32_bf16 a[20:23], v[0:3], v[26:29], a[20:23]
	s_nop 1
	v_mov_b32_e32 v0, v148
	v_mov_b32_e32 v1, v149
	v_mov_b32_e32 v2, v150
	v_mov_b32_e32 v3, v151
	v_accvgpr_write_b32 a39, v37
	v_accvgpr_write_b32 a38, v36
	v_mfma_f32_16x16x32_bf16 a[24:27], v[78:81], v[22:25], a[24:27]
	v_accvgpr_write_b32 a37, v35
	v_accvgpr_write_b32 a36, v34
	ds_read_b128 v[34:37], v44 offset:19456
	v_mfma_f32_16x16x32_bf16 a[24:27], v[50:53], v[10:13], a[24:27]
	ds_read_b128 v[50:53], v44 offset:15360
	v_pk_mul_f32 v[16:17], v[46:47], v[16:17] op_sel_hi:[0,1]
	s_waitcnt lgkmcnt(2)
	v_mfma_f32_16x16x32_bf16 a[24:27], v[4:7], v[26:29], a[24:27]
	ds_read_b128 v[4:7], v44 offset:16384
	v_pk_mul_f32 v[14:15], v[46:47], v[14:15] op_sel_hi:[0,1]
	v_accvgpr_write_b32 a51, v17
	v_mfma_f32_16x16x32_bf16 a[16:19], v[40:43], v[26:29], a[16:19]
	ds_read_b128 v[40:43], v44 offset:17408
	v_accvgpr_write_b32 a50, v16
	v_accvgpr_write_b32 a49, v15
	s_waitcnt lgkmcnt(1)
	v_mfma_f32_16x16x32_bf16 a[36:39], v[4:7], v[18:21], a[36:39]
	ds_read_b128 v[4:7], v44 offset:18432
	v_accvgpr_write_b32 a48, v14
	ds_read_b128 v[14:17], v44 offset:27648
	s_waitcnt lgkmcnt(2)
	v_mfma_f32_16x16x32_bf16 a[36:39], v[40:43], v[22:25], a[36:39]
	v_pk_mul_f32 v[2:3], v[46:47], v[2:3] op_sel_hi:[0,1]
	s_waitcnt lgkmcnt(1)
	v_mfma_f32_16x16x32_bf16 a[36:39], v[4:7], v[10:13], a[36:39]
	ds_read_b128 v[4:7], v44 offset:20480
	v_pk_mul_f32 v[0:1], v[46:47], v[0:1] op_sel_hi:[0,1]
	v_accvgpr_write_b32 a55, v3
	v_mfma_f32_16x16x32_bf16 a[36:39], v[34:37], v[26:29], a[36:39]
	ds_read_b128 v[34:37], v44 offset:21504
	v_accvgpr_write_b32 a54, v2
	v_accvgpr_write_b32 a53, v1
	s_waitcnt lgkmcnt(1)
	v_mfma_f32_16x16x32_bf16 a[44:47], v[4:7], v[18:21], a[44:47]
	ds_read_b128 v[4:7], v44 offset:22528
	v_accvgpr_write_b32 a52, v0
	ds_read_b128 v[0:3], v44 offset:30720
	s_waitcnt lgkmcnt(2)
	v_mfma_f32_16x16x32_bf16 a[44:47], v[34:37], v[22:25], a[44:47]
	v_accvgpr_read_b32 v9, a36
	s_waitcnt lgkmcnt(1)
	v_mfma_f32_16x16x32_bf16 a[44:47], v[4:7], v[10:13], a[44:47]
	ds_read_b128 v[4:7], v44 offset:24576
	v_mfma_f32_16x16x32_bf16 a[44:47], v[30:33], v[26:29], a[44:47]
	ds_read_b128 v[30:33], v44 offset:25600
	s_waitcnt lgkmcnt(1)
	v_mfma_f32_16x16x32_bf16 a[48:51], v[4:7], v[18:21], a[48:51]
	ds_read_b128 v[4:7], v44 offset:26624
	s_waitcnt lgkmcnt(1)
	v_mfma_f32_16x16x32_bf16 a[48:51], v[30:33], v[22:25], a[48:51]
	s_waitcnt lgkmcnt(0)
	v_mfma_f32_16x16x32_bf16 a[48:51], v[4:7], v[10:13], a[48:51]
	ds_read_b128 v[4:7], v44 offset:28672
	v_mfma_f32_16x16x32_bf16 a[48:51], v[14:17], v[26:29], a[48:51]
	ds_read_b128 v[14:17], v44 offset:29696
	s_waitcnt lgkmcnt(1)
	v_mfma_f32_16x16x32_bf16 a[52:55], v[4:7], v[18:21], a[52:55]
	ds_read_b128 v[4:7], v44 offset:31744
	s_nop 3
	v_accvgpr_read_b32 v20, a49
	s_waitcnt lgkmcnt(1)
	v_mfma_f32_16x16x32_bf16 a[52:55], v[14:17], v[22:25], a[52:55]
	v_accvgpr_read_b32 v16, a46
	v_accvgpr_read_b32 v21, a48
	v_cvt_pk_bf16_f32 v20, v21, v20
	v_mfma_f32_16x16x32_bf16 a[52:55], v[0:3], v[10:13], a[52:55]
	v_accvgpr_read_b32 v0, a17
	v_accvgpr_read_b32 v1, a16
	v_cvt_pk_bf16_f32 v0, v1, v0
	v_accvgpr_read_b32 v1, a19
	v_accvgpr_read_b32 v2, a18
	v_mfma_f32_16x16x32_bf16 a[28:31], v[50:53], v[26:29], a[28:31]
	v_cvt_pk_bf16_f32 v1, v2, v1
	v_accvgpr_read_b32 v2, a21
	v_accvgpr_read_b32 v3, a20
	s_waitcnt lgkmcnt(0)
	v_mfma_f32_16x16x32_bf16 a[52:55], v[4:7], v[26:29], a[52:55]
	v_cvt_pk_bf16_f32 v2, v3, v2
	v_accvgpr_read_b32 v3, a23
	v_accvgpr_read_b32 v4, a22
	v_cvt_pk_bf16_f32 v3, v4, v3
	v_accvgpr_read_b32 v4, a25
	v_accvgpr_read_b32 v5, a24
	v_cvt_pk_bf16_f32 v4, v5, v4
	v_accvgpr_read_b32 v5, a27
	v_accvgpr_read_b32 v6, a26
	v_cvt_pk_bf16_f32 v5, v6, v5
	v_accvgpr_read_b32 v6, a29
	v_accvgpr_read_b32 v7, a28
	v_cvt_pk_bf16_f32 v6, v7, v6
	v_accvgpr_read_b32 v7, a31
	v_accvgpr_read_b32 v8, a30
	v_cvt_pk_bf16_f32 v7, v8, v7
	v_accvgpr_read_b32 v8, a37
	ds_read_b128 v[12:15], v44 offset:32768
	v_cvt_pk_bf16_f32 v8, v9, v8
	v_accvgpr_read_b32 v9, a39
	v_accvgpr_read_b32 v10, a38
	v_cvt_pk_bf16_f32 v9, v10, v9
	v_accvgpr_read_b32 v10, a45
	v_accvgpr_read_b32 v11, a44
	v_cvt_pk_bf16_f32 v10, v11, v10
	v_accvgpr_read_b32 v11, a47
	v_cvt_pk_bf16_f32 v11, v16, v11
	ds_read_b128 v[16:19], v44 offset:33792
	ds_read_b128 v[24:27], v44 offset:34816
	s_waitcnt lgkmcnt(2)
	v_mfma_f32_16x16x32_bf16 a[0:3], v[12:15], v[0:3], a[0:3]
	v_accvgpr_read_b32 v21, a51
	v_accvgpr_read_b32 v12, a50
	v_cvt_pk_bf16_f32 v21, v12, v21
	ds_read_b128 v[12:15], v44 offset:35840
	s_waitcnt lgkmcnt(2)
	v_mfma_f32_16x16x32_bf16 a[0:3], v[16:19], v[4:7], a[0:3]
	v_accvgpr_read_b32 v16, a53
	v_accvgpr_read_b32 v17, a52
	v_cvt_pk_bf16_f32 v22, v17, v16
	s_waitcnt lgkmcnt(1)
	v_mfma_f32_16x16x32_bf16 a[0:3], v[24:27], v[8:11], a[0:3]
	v_accvgpr_read_b32 v16, a55
	v_accvgpr_read_b32 v17, a54
	v_accvgpr_write_b32 a16, v164
	v_accvgpr_write_b32 a17, v165
	v_accvgpr_write_b32 a18, v166
	v_accvgpr_write_b32 a19, v167
	v_cvt_pk_bf16_f32 v23, v17, v16
	v_accvgpr_write_b32 a20, v180
	v_accvgpr_write_b32 a21, v181
	v_accvgpr_write_b32 a22, v182
	v_accvgpr_write_b32 a23, v183
	s_waitcnt lgkmcnt(0)
	v_mfma_f32_16x16x32_bf16 a[0:3], v[12:15], v[20:23], a[0:3]
	s_nop 7
	v_accvgpr_read_b32 v12, a0
	v_mul_f32_e32 v12, 0x4038aa3b, v12
	v_exp_f32_e32 v16, v12
	v_accvgpr_read_b32 v12, a1
	v_mul_f32_e32 v12, 0x4038aa3b, v12
	v_exp_f32_e32 v17, v12
	ds_read_b128 v[12:15], v44 offset:36864
	v_add_f32_e32 v16, 1.0, v16
	v_rcp_f32_e32 v28, v16
	v_add_f32_e32 v24, 1.0, v17
	ds_read_b128 v[16:19], v44 offset:37888
	v_rcp_f32_e32 v29, v24
	ds_read_b128 v[24:27], v44 offset:38912
	s_waitcnt lgkmcnt(2)
	v_mfma_f32_16x16x32_bf16 a[24:27], v[12:15], v[0:3], a[56:59]
	v_accvgpr_read_b32 v30, a2
	v_mul_f32_e32 v12, 0x4038aa3b, v30
	v_exp_f32_e32 v30, v12
	ds_read_b128 v[12:15], v44 offset:39936
	s_waitcnt lgkmcnt(2)
	v_mfma_f32_16x16x32_bf16 a[24:27], v[16:19], v[4:7], a[24:27]
	v_accvgpr_read_b32 v16, a3
	v_mul_f32_e32 v16, 0x4038aa3b, v16
	v_exp_f32_e32 v17, v16
	s_waitcnt lgkmcnt(1)
	v_mfma_f32_16x16x32_bf16 a[0:3], v[24:27], v[8:11], a[24:27]
	v_add_f32_e32 v16, 1.0, v30
	v_rcp_f32_e32 v16, v16
	v_add_f32_e32 v17, 1.0, v17
	s_waitcnt lgkmcnt(0)
	v_mfma_f32_16x16x32_bf16 a[0:3], v[12:15], v[20:23], a[0:3]
	v_rcp_f32_e32 v17, v17
	v_pk_fma_f32 v[28:29], v[28:29], -2.0, 1.0 op_sel_hi:[1,0,0]
	v_pk_fma_f32 v[30:31], v[16:17], -2.0, 1.0 op_sel_hi:[1,0,0]
	s_nop 4
	v_accvgpr_read_b32 v12, a0
	v_mul_f32_e32 v12, 0x4038aa3b, v12
	v_accvgpr_read_b32 v13, a1
	v_exp_f32_e32 v12, v12
	v_mul_f32_e32 v13, 0x4038aa3b, v13
	v_exp_f32_e32 v13, v13
	v_accvgpr_read_b32 v35, a3
	v_add_f32_e32 v12, 1.0, v12
	v_rcp_f32_e32 v24, v12
	v_add_f32_e32 v18, 1.0, v13
	ds_read_b128 v[12:15], v44 offset:40960
	v_rcp_f32_e32 v25, v18
	ds_read_b128 v[16:19], v44 offset:41984
	s_waitcnt lgkmcnt(1)
	v_mfma_f32_16x16x32_bf16 a[4:7], v[12:15], v[0:3], a[4:7]
	v_fma_f32 v32, v24, -2.0, 1.0
	v_fma_f32 v33, v25, -2.0, 1.0
	v_accvgpr_read_b32 v24, a2
	v_mul_f32_e32 v34, 0x4038aa3b, v24
	ds_read_b128 v[24:27], v44 offset:43008
	ds_read_b128 v[12:15], v44 offset:44032
	s_waitcnt lgkmcnt(2)
	v_mfma_f32_16x16x32_bf16 a[0:3], v[16:19], v[4:7], a[4:7]
	v_mul_f32_e32 v16, 0x4038aa3b, v35
	v_exp_f32_e32 v16, v16
	v_exp_f32_e32 v34, v34
	s_waitcnt lgkmcnt(1)
	v_mfma_f32_16x16x32_bf16 a[0:3], v[24:27], v[8:11], a[0:3]
	v_add_f32_e32 v16, 1.0, v16
	v_rcp_f32_e32 v35, v16
	v_add_f32_e32 v17, 1.0, v34
	s_waitcnt lgkmcnt(0)
	v_mfma_f32_16x16x32_bf16 a[0:3], v[12:15], v[20:23], a[0:3]
	v_rcp_f32_e32 v34, v17
	v_accvgpr_write_b32 a4, v188
	v_accvgpr_write_b32 a5, v189
	v_accvgpr_write_b32 a6, v190
	v_accvgpr_write_b32 a7, v191
	v_pk_fma_f32 v[34:35], v[34:35], -2.0, 1.0 op_sel_hi:[1,0,0]
	s_nop 4
	v_accvgpr_read_b32 v12, a0
	v_mul_f32_e32 v12, 0x4038aa3b, v12
	v_exp_f32_e32 v16, v12
	v_accvgpr_read_b32 v12, a1
	v_mul_f32_e32 v12, 0x4038aa3b, v12
	v_exp_f32_e32 v17, v12
	ds_read_b128 v[12:15], v44 offset:45056
	v_add_f32_e32 v16, 1.0, v16
	v_rcp_f32_e32 v36, v16
	v_add_f32_e32 v24, 1.0, v17
	ds_read_b128 v[16:19], v44 offset:46080
	v_rcp_f32_e32 v37, v24
	ds_read_b128 v[24:27], v44 offset:47104
	s_waitcnt lgkmcnt(2)
	v_mfma_f32_16x16x32_bf16 a[16:19], v[12:15], v[0:3], a[16:19]
	v_accvgpr_read_b32 v38, a2
	v_mul_f32_e32 v12, 0x4038aa3b, v38
	v_exp_f32_e32 v38, v12
	ds_read_b128 v[12:15], v44 offset:48128
	s_waitcnt lgkmcnt(2)
	v_mfma_f32_16x16x32_bf16 a[16:19], v[16:19], v[4:7], a[16:19]
	v_accvgpr_read_b32 v17, a3
	v_mul_f32_e32 v17, 0x4038aa3b, v17
	v_exp_f32_e32 v17, v17
	s_waitcnt lgkmcnt(1)
	v_mfma_f32_16x16x32_bf16 a[16:19], v[24:27], v[8:11], a[16:19]
	v_add_f32_e32 v16, 1.0, v38
	v_rcp_f32_e32 v38, v16
	v_pk_fma_f32 v[36:37], v[36:37], -2.0, 1.0 op_sel_hi:[1,0,0]
	s_waitcnt lgkmcnt(0)
	v_mfma_f32_16x16x32_bf16 a[0:3], v[12:15], v[20:23], a[16:19]
	v_add_f32_e32 v13, 1.0, v17
	v_rcp_f32_e32 v39, v13
	s_nop 0
	v_pk_fma_f32 v[38:39], v[38:39], -2.0, 1.0 op_sel_hi:[1,0,0]
	s_nop 3
	v_accvgpr_read_b32 v12, a0
	v_mul_f32_e32 v12, 0x4038aa3b, v12
	v_exp_f32_e32 v12, v12
	v_accvgpr_read_b32 v17, a2
	v_mul_f32_e32 v17, 0x4038aa3b, v17
	v_exp_f32_e32 v24, v17
	v_add_f32_e32 v12, 1.0, v12
	v_rcp_f32_e32 v40, v12
	v_accvgpr_read_b32 v12, a1
	v_mul_f32_e32 v12, 0x4038aa3b, v12
	v_exp_f32_e32 v16, v12
	ds_read_b128 v[12:15], v44 offset:49152
	v_add_f32_e32 v42, 1.0, v24
	v_accvgpr_read_b32 v43, a3
	v_add_f32_e32 v25, 1.0, v16
	ds_read_b128 v[16:19], v44 offset:50176
	v_rcp_f32_e32 v41, v25
	ds_read_b128 v[24:27], v44 offset:51200
	s_waitcnt lgkmcnt(2)
	v_mfma_f32_16x16x32_bf16 a[0:3], v[12:15], v[0:3], a[32:35]
	v_mul_f32_e32 v12, 0x4038aa3b, v43
	v_exp_f32_e32 v43, v12
	ds_read_b128 v[12:15], v44 offset:52224
	s_waitcnt lgkmcnt(2)
	v_mfma_f32_16x16x32_bf16 a[0:3], v[16:19], v[4:7], a[0:3]
	v_rcp_f32_e32 v16, v42
	v_add_f32_e32 v17, 1.0, v43
	v_rcp_f32_e32 v17, v17
	s_waitcnt lgkmcnt(1)
	v_mfma_f32_16x16x32_bf16 a[0:3], v[24:27], v[8:11], a[0:3]
	v_fma_f32 v40, v40, -2.0, 1.0
	v_fma_f32 v41, v41, -2.0, 1.0
	v_pk_fma_f32 v[42:43], v[16:17], -2.0, 1.0 op_sel_hi:[1,0,0]
	s_waitcnt lgkmcnt(0)
	v_mfma_f32_16x16x32_bf16 a[0:3], v[12:15], v[20:23], a[0:3]
	s_nop 7
	v_accvgpr_read_b32 v12, a0
	v_mul_f32_e32 v12, 0x4038aa3b, v12
	v_exp_f32_e32 v16, v12
	v_accvgpr_read_b32 v12, a1
	v_mul_f32_e32 v17, 0x4038aa3b, v12
	ds_read_b128 v[12:15], v44 offset:53248
	v_exp_f32_e32 v24, v17
	v_add_f32_e32 v16, 1.0, v16
	v_rcp_f32_e32 v50, v16
	ds_read_b128 v[16:19], v44 offset:54272
	v_add_f32_e32 v24, 1.0, v24
	v_rcp_f32_e32 v51, v24
	ds_read_b128 v[24:27], v44 offset:55296
	s_waitcnt lgkmcnt(2)
	v_mfma_f32_16x16x32_bf16 a[16:19], v[12:15], v[0:3], a[40:43]
	v_accvgpr_read_b32 v52, a2
	v_mul_f32_e32 v0, 0x4038aa3b, v52
	v_exp_f32_e32 v12, v0
	ds_read_b128 v[0:3], v44 offset:56320
	s_waitcnt lgkmcnt(2)
	v_mfma_f32_16x16x32_bf16 a[16:19], v[16:19], v[4:7], a[16:19]
	v_accvgpr_read_b32 v4, a3
	v_mul_f32_e32 v4, 0x4038aa3b, v4
	v_exp_f32_e32 v5, v4
	s_waitcnt lgkmcnt(1)
	v_mfma_f32_16x16x32_bf16 a[0:3], v[24:27], v[8:11], a[16:19]
	v_add_f32_e32 v4, 1.0, v12
	ds_read_b128 v[10:13], v44 offset:57344
	v_add_f32_e32 v5, 1.0, v5
	s_waitcnt lgkmcnt(1)
	v_mfma_f32_16x16x32_bf16 a[0:3], v[0:3], v[20:23], a[0:3]
	v_rcp_f32_e32 v4, v4
	v_rcp_f32_e32 v5, v5
	ds_read_b128 v[18:21], v44 offset:58368
	v_pk_fma_f32 v[14:15], v[50:51], -2.0, 1.0 op_sel_hi:[1,0,0]
	v_cvt_pk_bf16_f32 v6, v36, v37
	v_pk_fma_f32 v[16:17], v[4:5], -2.0, 1.0 op_sel_hi:[1,0,0]
	v_cvt_pk_bf16_f32 v4, v32, v33
	v_cvt_pk_bf16_f32 v5, v34, v35
	v_accvgpr_read_b32 v2, a2
	v_accvgpr_read_b32 v3, a3
	v_mul_f32_e32 v2, 0x4038aa3b, v2
	v_mul_f32_e32 v3, 0x4038aa3b, v3
	v_exp_f32_e32 v2, v2
	v_exp_f32_e32 v3, v3
	v_accvgpr_read_b32 v0, a0
	v_accvgpr_read_b32 v1, a1
	v_add_f32_e32 v2, 1.0, v2
	v_add_f32_e32 v3, 1.0, v3
	v_rcp_f32_e32 v2, v2
	v_rcp_f32_e32 v3, v3
	v_mul_f32_e32 v0, 0x4038aa3b, v0
	v_mul_f32_e32 v1, 0x4038aa3b, v1
	v_exp_f32_e32 v0, v0
	v_exp_f32_e32 v1, v1
	v_pk_fma_f32 v[22:23], v[2:3], -2.0, 1.0 op_sel_hi:[1,0,0]
	v_cvt_pk_bf16_f32 v2, v28, v29
	v_cvt_pk_bf16_f32 v3, v30, v31
	v_cvt_pk_bf16_f32 v14, v14, v15
	v_cvt_pk_bf16_f32 v15, v16, v17
	v_cvt_pk_bf16_f32 v17, v22, v23
	ds_read_b128 v[22:25], v44 offset:59392
	s_waitcnt lgkmcnt(2)
	v_mfma_f32_16x16x32_bf16 a[0:3], v[10:13], v[2:5], a[8:11]
	ds_read_b128 v[10:13], v44 offset:60416
	v_add_f32_e32 v0, 1.0, v0
	v_add_f32_e32 v1, 1.0, v1
	v_rcp_f32_e32 v0, v0
	v_rcp_f32_e32 v1, v1
	v_cvt_pk_bf16_f32 v7, v38, v39
	v_cvt_pk_bf16_f32 v8, v40, v41
	v_cvt_pk_bf16_f32 v9, v42, v43
	v_pk_fma_f32 v[0:1], v[0:1], -2.0, 1.0 op_sel_hi:[1,0,0]
	s_waitcnt lgkmcnt(0)
	v_mfma_f32_16x16x32_bf16 a[8:11], v[10:13], v[2:5], a[20:23]
	v_cvt_pk_bf16_f32 v16, v0, v1
	v_mov_b32_e32 v0, 0x11000
	v_mad_u32_u24 v0, v56, s0, v0
	v_mfma_f32_16x16x32_bf16 a[0:3], v[18:21], v[6:9], a[0:3]
	ds_read_b128 v[18:21], v44 offset:61440
	v_mad_u32_u24 v1, v57, s2, v0
	v_add_u32_e32 v26, v1, v48
	v_mfma_f32_16x16x32_bf16 a[0:3], v[22:25], v[14:17], a[0:3]
	ds_read_b128 v[22:25], v44 offset:62464
	s_waitcnt lgkmcnt(1)
	v_mfma_f32_16x16x32_bf16 a[8:11], v[18:21], v[6:9], a[8:11]
	ds_read_b128 v[18:21], v44 offset:64512
	s_nop 3
	v_accvgpr_read_b32 v27, a1
	v_accvgpr_read_b32 v10, a0
	ds_write2_b32 v26, v10, v27 offset0:1 offset1:2
	v_accvgpr_read_b32 v10, a3
	v_accvgpr_read_b32 v11, a2
	ds_write2_b32 v26, v11, v10 offset0:3 offset1:4
	ds_read_b128 v[10:13], v44 offset:63488
	s_waitcnt lgkmcnt(4)
	v_mfma_f32_16x16x32_bf16 a[0:3], v[22:25], v[14:17], a[8:11]
	s_nop 7
	v_accvgpr_read_b32 v22, a1
	v_accvgpr_read_b32 v23, a0
	ds_write2_b32 v26, v23, v22 offset0:17 offset1:18
	v_or_b32_e32 v22, 0x10000, v44
	ds_read_b128 v[22:25], v22
	s_waitcnt lgkmcnt(2)
	v_mfma_f32_16x16x32_bf16 a[8:11], v[10:13], v[2:5], a[12:15]
	v_or_b32_e32 v10, 0x10400, v44
	ds_read_b128 v[10:13], v10
	v_accvgpr_read_b32 v27, a3
	v_mfma_f32_16x16x32_bf16 a[8:11], v[18:21], v[6:9], a[8:11]
	v_or_b32_e32 v18, 0x10800, v44
	ds_read_b128 v[18:21], v18
	v_accvgpr_read_b32 v28, a2
	s_waitcnt lgkmcnt(2)
	v_mfma_f32_16x16x32_bf16 a[0:3], v[22:25], v[14:17], a[8:11]
	v_or_b32_e32 v22, 0x10c00, v44
	ds_read_b128 v[22:25], v22
	ds_write2_b32 v26, v28, v27 offset0:19 offset1:20
	s_waitcnt lgkmcnt(3)
	v_mfma_f32_16x16x32_bf16 a[4:7], v[10:13], v[2:5], a[4:7]
	s_waitcnt lgkmcnt(2)
	v_mfma_f32_16x16x32_bf16 a[4:7], v[18:21], v[6:9], a[4:7]
	s_nop 0
	v_accvgpr_read_b32 v2, a1
	v_accvgpr_read_b32 v3, a0
	ds_write2_b32 v26, v3, v2 offset0:33 offset1:34
	v_accvgpr_read_b32 v2, a3
	v_accvgpr_read_b32 v3, a2
	s_waitcnt lgkmcnt(2)
	v_mfma_f32_16x16x32_bf16 a[0:3], v[22:25], v[14:17], a[4:7]
	ds_write2_b32 v26, v3, v2 offset0:35 offset1:36
	s_nop 6
	v_accvgpr_read_b32 v2, a1
	v_accvgpr_read_b32 v3, a0
	ds_write2_b32 v26, v3, v2 offset0:49 offset1:50
	v_accvgpr_read_b32 v2, a3
	v_accvgpr_read_b32 v3, a2
	ds_write2_b32 v26, v3, v2 offset0:51 offset1:52
	s_and_saveexec_b64 s[0:1], vcc
	ds_write_b32 v1, v46
	s_or_b64 exec, exec, s[0:1]
	v_add_u32_e32 v2, v0, v44
	v_mov_b64_e32 v[0:1], s[10:11]
	v_mad_u64_u32 v[0:1], s[0:1], v47, s2, v[0:1]
	ds_read_b128 v[4:7], v2
	v_lshl_add_u64 v[8:9], v[0:1], 0, v[44:45]
	s_waitcnt lgkmcnt(0)
	global_store_dwordx4 v[8:9], v[4:7], off sc1
	s_nop 1
	s_mov_b64 s[0:1], 0x400
	ds_read_b128 v[4:7], v2 offset:1024
	v_lshl_add_u64 v[10:11], v[8:9], 0, s[0:1]
	s_waitcnt lgkmcnt(0)
	global_store_dwordx4 v[10:11], v[4:7], off sc1
	s_nop 1
	s_mov_b64 s[0:1], 0x800
	ds_read_b128 v[4:7], v2 offset:2048
	v_lshl_add_u64 v[10:11], v[8:9], 0, s[0:1]
	s_waitcnt lgkmcnt(0)
	global_store_dwordx4 v[10:11], v[4:7], off sc1
	s_nop 1
	s_mov_b64 s[0:1], 0xc00
	ds_read_b128 v[4:7], v2 offset:3072
	v_lshl_add_u64 v[8:9], v[8:9], 0, s[0:1]
	s_waitcnt lgkmcnt(0)
	global_store_dwordx4 v[8:9], v[4:7], off sc1
	s_nop 1
	v_or_b32_e32 v3, 0x100, v49
	v_cmp_gt_u32_e32 vcc, s2, v3
	s_and_saveexec_b64 s[0:1], vcc
	s_cbranch_execz .LBB2_4
	ds_read_b128 v[4:7], v2 offset:4096
	v_lshlrev_b32_e32 v2, 4, v3
	v_mov_b32_e32 v3, 0
	v_lshl_add_u64 v[0:1], v[0:1], 0, v[2:3]
	s_waitcnt lgkmcnt(0)
	global_store_dwordx4 v[0:1], v[4:7], off sc1
	s_nop 1

	.amdhsa_kernel _Z10enc_kernelPKfS0_PK15HIP_vector_typeIjLj4EES4_S4_S0_S0_S0_Pf
		.amdhsa_group_segment_fixed_size 86272
		.amdhsa_private_segment_fixed_size 0
		.amdhsa_kernarg_size 72
		.amdhsa_user_sgpr_count 2
		.amdhsa_user_sgpr_dispatch_ptr 0
		.amdhsa_user_sgpr_queue_ptr 0
		.amdhsa_user_sgpr_kernarg_segment_ptr 1
		.amdhsa_user_sgpr_dispatch_id 0
		.amdhsa_user_sgpr_kernarg_preload_length 0
		.amdhsa_user_sgpr_kernarg_preload_offset 0
		.amdhsa_user_sgpr_private_segment_size 0
		.amdhsa_uses_dynamic_stack 0
		.amdhsa_enable_private_segment 0
		.amdhsa_system_sgpr_workgroup_id_x 1
		.amdhsa_system_sgpr_workgroup_id_y 0
		.amdhsa_system_sgpr_workgroup_id_z 0
		.amdhsa_system_sgpr_workgroup_info 0
		.amdhsa_system_vgpr_workitem_id 0
		.amdhsa_next_free_vgpr 257
		.amdhsa_next_free_sgpr 96
		.amdhsa_accum_offset 192
		.amdhsa_reserve_vcc 1
		.amdhsa_float_round_mode_32 0
		.amdhsa_float_round_mode_16_64 0
		.amdhsa_float_denorm_mode_32 3
		.amdhsa_float_denorm_mode_16_64 3
		.amdhsa_dx10_clamp 1
		.amdhsa_ieee_mode 1
		.amdhsa_fp16_overflow 0
		.amdhsa_tg_split 0
		.amdhsa_exception_fp_ieee_invalid_op 0
		.amdhsa_exception_fp_denorm_src 0
		.amdhsa_exception_fp_ieee_div_zero 0
		.amdhsa_exception_fp_ieee_overflow 0
		.amdhsa_exception_fp_ieee_underflow 0
		.amdhsa_exception_fp_ieee_inexact 0
		.amdhsa_exception_int_div_zero 0
	.end_amdhsa_kernel

amdhsa.kernels:
  - .agpr_count:     0
    .args:
      - .actual_access:  read_only
        .address_space:  global
        .offset:         0
        .size:           8
        .value_kind:     global_buffer
      - .actual_access:  read_only
        .address_space:  global
        .offset:         8
        .size:           8
        .value_kind:     global_buffer
      - .actual_access:  read_only
        .address_space:  global
        .offset:         16
        .size:           8
        .value_kind:     global_buffer
      - .actual_access:  read_only
        .address_space:  global
        .offset:         24
        .size:           8
        .value_kind:     global_buffer
      - .actual_access:  read_only
        .address_space:  global
        .offset:         32
        .size:           8
        .value_kind:     global_buffer
      - .actual_access:  read_only
        .address_space:  global
        .offset:         40
        .size:           8
        .value_kind:     global_buffer
      - .actual_access:  read_only
        .address_space:  global
        .offset:         48
        .size:           8
        .value_kind:     global_buffer
      - .actual_access:  read_only
        .address_space:  global
        .offset:         56
        .size:           8
        .value_kind:     global_buffer
      - .address_space:  global
        .offset:         64
        .size:           8
        .value_kind:     global_buffer
      - .offset:         72
        .size:           4
        .value_kind:     hidden_block_count_x
      - .offset:         76
        .size:           4
        .value_kind:     hidden_block_count_y
      - .offset:         80
        .size:           4
        .value_kind:     hidden_block_count_z
      - .offset:         84
        .size:           2
        .value_kind:     hidden_group_size_x
      - .offset:         86
        .size:           2
        .value_kind:     hidden_group_size_y
      - .offset:         88
        .size:           2
        .value_kind:     hidden_group_size_z
      - .offset:         90
        .size:           2
        .value_kind:     hidden_remainder_x
      - .offset:         92
        .size:           2
        .value_kind:     hidden_remainder_y
      - .offset:         94
        .size:           2
        .value_kind:     hidden_remainder_z
      - .offset:         112
        .size:           8
        .value_kind:     hidden_global_offset_x
      - .offset:         120
        .size:           8
        .value_kind:     hidden_global_offset_y
      - .offset:         128
        .size:           8
        .value_kind:     hidden_global_offset_z
      - .offset:         136
        .size:           2
        .value_kind:     hidden_grid_dims
    .group_segment_fixed_size: 256
    .kernarg_segment_align: 8
    .kernarg_segment_size: 328
    .language:       OpenCL C
    .language_version:
      - 2
      - 0
    .max_flat_workgroup_size: 256
    .name:           _Z11prep_kernelPKfS0_S0_S0_S0_S0_S0_PKiPc
    .private_segment_fixed_size: 0
    .sgpr_count:     58
    .sgpr_spill_count: 0
    .symbol:         _Z11prep_kernelPKfS0_S0_S0_S0_S0_S0_PKiPc.kd
    .uniform_work_group_size: 1
    .uses_dynamic_stack: false
    .vgpr_count:     37
    .vgpr_spill_count: 0
    .wavefront_size: 64
  - .agpr_count:     0
    .args:
      - .actual_access:  read_only
        .address_space:  global
        .offset:         0
        .size:           8
        .value_kind:     global_buffer
      - .address_space:  global
        .offset:         8
        .size:           8
        .value_kind:     global_buffer
      - .actual_access:  read_only
        .address_space:  global
        .offset:         16
        .size:           8
        .value_kind:     global_buffer
      - .actual_access:  read_only
        .address_space:  global
        .offset:         24
        .size:           8
        .value_kind:     global_buffer
      - .address_space:  global
        .offset:         32
        .size:           8
        .value_kind:     global_buffer
      - .address_space:  global
        .offset:         40
        .size:           8
        .value_kind:     global_buffer
      - .actual_access:  read_only
        .address_space:  global
        .offset:         48
        .size:           8
        .value_kind:     global_buffer
      - .offset:         56
        .size:           4
        .value_kind:     by_value
      - .offset:         64
        .size:           4
        .value_kind:     hidden_block_count_x
      - .offset:         68
        .size:           4
        .value_kind:     hidden_block_count_y
      - .offset:         72
        .size:           4
        .value_kind:     hidden_block_count_z
      - .offset:         76
        .size:           2
        .value_kind:     hidden_group_size_x
      - .offset:         78
        .size:           2
        .value_kind:     hidden_group_size_y
      - .offset:         80
        .size:           2
        .value_kind:     hidden_group_size_z
      - .offset:         82
        .size:           2
        .value_kind:     hidden_remainder_x
      - .offset:         84
        .size:           2
        .value_kind:     hidden_remainder_y
      - .offset:         86
        .size:           2
        .value_kind:     hidden_remainder_z
      - .offset:         104
        .size:           8
        .value_kind:     hidden_global_offset_x
      - .offset:         112
        .size:           8
        .value_kind:     hidden_global_offset_y
      - .offset:         120
        .size:           8
        .value_kind:     hidden_global_offset_z
      - .offset:         128
        .size:           2
        .value_kind:     hidden_grid_dims
    .group_segment_fixed_size: 135936
    .kernarg_segment_align: 8
    .kernarg_segment_size: 320
    .language:       OpenCL C
    .language_version:
      - 2
      - 0
    .max_flat_workgroup_size: 768
    .name:           _Z11main_kernelPKfPKiPK15HIP_vector_typeIjLj4EES0_PfS7_S2_i
    .private_segment_fixed_size: 0
    .sgpr_count:     66
    .sgpr_spill_count: 0
    .symbol:         _Z11main_kernelPKfPKiPK15HIP_vector_typeIjLj4EES0_PfS7_S2_i.kd
    .uniform_work_group_size: 1
    .uses_dynamic_stack: false
    .vgpr_count:     156
    .vgpr_spill_count: 0
    .wavefront_size: 64
  - .agpr_count:     60
    .args:
      - .actual_access:  read_only
        .address_space:  global
        .offset:         0
        .size:           8
        .value_kind:     global_buffer
      - .actual_access:  read_only
        .address_space:  global
        .offset:         8
        .size:           8
        .value_kind:     global_buffer
      - .actual_access:  read_only
        .address_space:  global
        .offset:         16
        .size:           8
        .value_kind:     global_buffer
      - .actual_access:  read_only
        .address_space:  global
        .offset:         24
        .size:           8
        .value_kind:     global_buffer
      - .actual_access:  read_only
        .address_space:  global
        .offset:         32
        .size:           8
        .value_kind:     global_buffer
      - .actual_access:  read_only
        .address_space:  global
        .offset:         40
        .size:           8
        .value_kind:     global_buffer
      - .actual_access:  read_only
        .address_space:  global
        .offset:         48
        .size:           8
        .value_kind:     global_buffer
      - .actual_access:  read_only
        .address_space:  global
        .offset:         56
        .size:           8
        .value_kind:     global_buffer
      - .address_space:  global
        .offset:         64
        .size:           8
        .value_kind:     global_buffer
    .group_segment_fixed_size: 86272
    .kernarg_segment_align: 8
    .kernarg_segment_size: 72
    .language:       OpenCL C
    .language_version:
      - 2
      - 0
    .max_flat_workgroup_size: 256
    .name:           _Z10enc_kernelPKfS0_PK15HIP_vector_typeIjLj4EES4_S4_S0_S0_S0_Pf
    .private_segment_fixed_size: 0
    .sgpr_count:     24
    .sgpr_spill_count: 0
    .symbol:         _Z10enc_kernelPKfS0_PK15HIP_vector_typeIjLj4EES4_S4_S0_S0_S0_Pf.kd
    .uniform_work_group_size: 1
    .uses_dynamic_stack: false
    .vgpr_count:     252
    .vgpr_spill_count: 0
    .wavefront_size: 64
